# leftover conversion tiles (16 per layer) moved to workgroups with slack: layer-0 ones at the attention phase start, layer-1 ones in the last MoE sub-phase; prologue now 2 equal rounds
# speedup vs baseline: 1.0314x; 1.0042x over previous
; #define LAS __attribute__((address_space(3)))
; __device__ __forceinline__ void wg_convert_layer(Frame& F, int l) {
;     __syncthreads();
;     for (int it = F.gw >> 3; it < WG_ITEMS_PER_LAYER; it += F.G) wg_conv_item(F, l, it);
; }
; __device__ __forceinline__ void p0_prologue(Frame& F) {
;     LAS float* scr = (LAS float*)(F.lds + F.wave * 16384);
;     wg_convert_layer(F, 0);
.LBB0_8:
	s_or_b64 exec, exec, s[6:7]
	s_load_dwordx2 s[74:75], s[92:93], 0xe8
	s_lshl_b32 s6, s10, 3
	v_readlane_b32 s7, v251, 2
	s_add_i32 s6, s6, s7
	s_lshl_b32 s84, s68, 3
	v_writelane_b32 v251, s6, 3
	s_waitcnt lgkmcnt(0)
	s_cmp_lt_i32 s74, 1
	v_writelane_b32 v251, s87, 4
	s_cselect_b64 s[6:7], -1, 0
	s_cmp_gt_i32 s75, 0
	v_writelane_b32 v251, s72, 5
	s_cselect_b64 s[8:9], -1, 0
	s_and_b64 s[12:13], s[6:7], s[8:9]
	v_writelane_b32 v251, s73, 6
	v_writelane_b32 v251, s74, 7
	s_and_b64 vcc, exec, s[12:13]
	s_nop 0
	v_writelane_b32 v251, s75, 8
	s_cbranch_vccz .LBB0_225
	v_readlane_b32 s6, v251, 3
	s_ashr_i32 s30, s6, 3
	s_mov_b32 s94, s68
	s_mov_b32 s90, s84
	s_cmpk_gt_i32 s30, 0x1ff
	s_barrier
	s_cbranch_scc1 .LBB0_161
	s_add_u32 s31, s0, 0x18500000
	v_readlane_b32 s6, v251, 2
	s_addc_u32 s34, s1, 0
	s_lshl_b32 s35, s6, 3
	s_add_i32 s36, s6, 8
	s_add_i32 s37, s6, 16
	s_add_i32 s38, s6, 24
	s_add_u32 s39, s0, 0x8500000
	s_load_dwordx2 s[8:9], s[92:93], 0x98
	s_load_dwordx2 s[10:11], s[92:93], 0xd0
	s_load_dwordx2 s[14:15], s[92:93], 0x58
	s_addc_u32 s40, s1, 0
	s_add_u32 s41, s0, 0x100000
	s_addc_u32 s42, s1, 0
	s_load_dwordx2 s[18:19], s[92:93], 0x18
	s_waitcnt lgkmcnt(0)
	s_cmp_lg_u64 s[8:9], 0
	s_cselect_b64 s[16:17], -1, 0
	s_cmp_eq_u64 s[14:15], 0
	s_cselect_b64 s[20:21], -1, 0
	s_lshl_b32 s6, s30, 5
	s_lshl_b32 s43, s30, 8
	s_lshl_b32 s44, s94, 8
	s_add_i32 s45, s6, 0xffffe600
	s_lshl_b32 s46, s94, 5
	s_movk_i32 s47, 0x2000
	s_movk_i32 s48, 0x4000
	s_movk_i32 s49, 0x6000
	s_mov_b32 s50, 0x8000
	s_mov_b32 s51, 0xa000
	s_mov_b32 s52, 0xc000
	s_mov_b32 s53, 0xe000
	s_mov_b32 s54, 0x80000
	s_mov_b32 s55, 0x82000
	s_mov_b32 s56, 0x84000
	s_mov_b32 s57, 0x86000
	s_mov_b32 s58, 0x88000
	s_mov_b32 s59, 0x100000
	s_mov_b32 s60, 0x102000
	s_mov_b32 s61, 0x104000
	s_mov_b32 s62, 0x106000
	s_mov_b32 s63, 0x108000
	s_mov_b32 s64, 0x180000
	s_mov_b32 s65, 0x182000
	s_mov_b32 s66, 0x184000
	s_mov_b32 s67, 0x186000
	s_mov_b32 s68, 0x188000
	v_mov_b32_e32 v67, 0
	s_mov_b32 s69, 0x20000
	s_mov_b32 s70, 0x1ce000
	s_mov_b32 s71, 0x341000
	s_mov_b32 s72, 0x347000
	s_mov_b32 s73, 0x34e000
	s_mov_b32 s74, 0x354000
	s_mov_b32 s75, 0x35b000
	s_mov_b32 s76, 0x361000
	s_mov_b32 s77, 0x368000
	s_mov_b32 s78, 0x36e000
	s_mov_b32 s79, 0x4e1000
	s_mov_b32 s80, 0x4e8000
	s_mov_b32 s81, 0x4ee000
	s_mov_b32 s82, 0x4f5000
	s_mov_b32 s83, 0x4fb000
	s_mov_b32 s84, 0x502000
	s_mov_b32 s85, 0x508000
	s_mov_b32 s86, 0x50f000
	s_mov_b32 s23, 0
	s_branch .LBB0_12
.LBB0_11:
	s_add_i32 s30, s30, s94
	s_add_i32 s43, s43, s44
	s_add_i32 s45, s45, s46
	s_cmpk_lt_i32 s30, 0x200
	s_cbranch_scc0 .LBB0_161

; #define INL(j) (((MK_PHMASK >> (j)) & 1) && INR(pb + (j)))
; __device__ __forceinline__ void wg_convert_layer(Frame& F, int l) {
;     __syncthreads();
;     for (int it = F.gw >> 3; it < WG_ITEMS_PER_LAYER; it += F.G) wg_conv_item(F, l, it);
; }
; __global__ void __launch_bounds__(NTHR, 2) mega_fwd(Args args) {
;     ...
;         if (INL(0)) { if (l == 1) wg_convert_layer(F, 1);
.LBB0_290:
	s_andn2_b64 vcc, exec, s[4:5]
	s_cbranch_vccnz .LBB0_450
	v_readlane_b32 s16, v248, 1
	s_ashr_i32 s50, s76, 3
	s_addk_i32 s50, 0x900
	v_readlane_b32 s17, v248, 2
	s_cmpk_gt_i32 s50, 0x80f
	v_readlane_b32 s0, v250, 10
	v_readlane_b32 s1, v251, 11
	v_readlane_b32 s15, v251, 12
	v_readlane_b32 s17, v251, 13
	s_mov_b32 s67, 0x8002000
	s_barrier
	s_cbranch_scc1 .LBB0_445
	s_add_u32 s51, s44, 0x1c500000
	s_addc_u32 s58, s45, 0
	s_add_u32 s59, s44, 0x10500000
	s_addc_u32 s60, s45, 0
	s_add_u32 s61, s44, 0x1b00000
	s_addc_u32 s62, s45, 0
	s_lshl_b32 s4, s50, 5
	s_lshl_b32 s63, s50, 8
	s_lshl_b32 s64, s16, 8
	s_add_i32 s65, s4, 0xffffe600
	s_lshl_b32 s66, s16, 5
	s_branch .LBB0_294

; #define INL(j) (((MK_PHMASK >> (j)) & 1) && INR(pb + (j)))
; __global__ void __launch_bounds__(NTHR, 2) mega_fwd(Args args) {
;     ...
;         if (INL(4)) {
;             {
;                 const int nsc = F.G == 256 ? 64 : F.G, sc0 = F.G - nsc;
;                 if (bx >= sc0) {
;                     for (int B = bx - sc0; B < 256; B += nsc) hg_scan_item(F, B);
;                     asm volatile("s_waitcnt vmcnt(0)" ::: "memory"); __syncthreads();
;                     if (F.tid == 0) { __builtin_amdgcn_fence(__ATOMIC_RELEASE, "agent"); asm volatile("s_waitcnt vmcnt(0)" ::: "memory"); __hip_atomic_fetch_add(F.ctl + CW_SCN + l * 64, 1u, RLX_AGENT); }
;                 }
.LBB0_771:
	s_cmp_lg_u32 s101, 3
	s_cbranch_scc1 .Lcv_ret_8
	v_readlane_b32 s100, v251, 3
	s_nop 3
	s_and_b32 s100, s100, 0xf0
	s_cmp_lg_u32 s100, 0xa0
	s_cbranch_scc1 .Lcv_ret_8
	s_mov_b32 s100, 16777224
	s_branch .Lcv_run

; #define LAS __attribute__((address_space(3)))
; __device__ __forceinline__ int lane_id_v() { int l; asm volatile("v_mbcnt_lo_u32_b32 %0, -1, 0\n\tv_mbcnt_hi_u32_b32 %0, -1, %0" : "=v"(l)); return l; }
; __device__ __forceinline__ void wg_convert_tile(Frame& F, const float* W, int ldw, bf16_t* WT, int Kd, int k0, int n0, int kind, const float* kgain) {
;     const int lane = lane_id_v(), w = F.wave;
;     LAS unsigned char* img = F.lds;
;     const float* src = W + (size_t)(k0 + 8 * w) * ldw + n0 + 4 * lane;
.Lcv_run:
	v_writelane_b32 v253, s6, 0
	v_writelane_b32 v253, s7, 1
	v_writelane_b32 v253, s8, 2
	v_writelane_b32 v253, s9, 3
	v_writelane_b32 v253, s11, 4
	v_writelane_b32 v253, s12, 5
	v_writelane_b32 v253, s13, 6
	v_writelane_b32 v253, s14, 7
	v_writelane_b32 v253, s32, 8
	v_writelane_b32 v253, s38, 9
	v_writelane_b32 v253, s39, 10
	v_writelane_b32 v253, s55, 11
	v_writelane_b32 v253, s56, 12
	v_writelane_b32 v253, s57, 13
	v_writelane_b32 v253, s58, 14
	v_writelane_b32 v253, s59, 15
	v_writelane_b32 v253, s60, 16
	v_writelane_b32 v253, s61, 17
	v_writelane_b32 v253, s62, 18
	v_writelane_b32 v253, s63, 19
	v_writelane_b32 v253, s64, 20
	v_writelane_b32 v253, s65, 21
	v_writelane_b32 v253, s67, 22
	v_writelane_b32 v253, s70, 23
	v_writelane_b32 v253, s71, 24
	v_writelane_b32 v253, s76, 25
	v_writelane_b32 v253, s80, 26
	v_writelane_b32 v253, s81, 27
	v_writelane_b32 v253, s83, 28
	v_writelane_b32 v253, s95, 29
	v_writelane_b32 v253, s96, 30
	v_writelane_b32 v253, s97, 31
	v_writelane_b32 v253, s98, 32
	v_writelane_b32 v253, s99, 33
	v_readlane_b32 s6, v251, 9
	v_readlane_b32 s7, v251, 10
	v_readlane_b32 s8, v251, 2
	v_readlane_b32 s9, v251, 3
	v_mbcnt_lo_u32_b32 v2, -1, 0
	v_mbcnt_hi_u32_b32 v2, -1, v2
	s_nop 3
	s_lshr_b32 s9, s9, 3
	s_load_dwordx2 s[12:13], s[6:7], 0xe0
	v_lshlrev_b32_e32 v3, 4, v2
	v_and_b32_e32 v14, 31, v2
	v_lshrrev_b32_e32 v15, 5, v2
	v_lshl_add_u32 v16, s8, 1, v15
	v_mov_b32_e32 v17, 0
	s_bfe_u32 s11, s100, 0x80008
	s_sub_i32 s11, s11, s101
	s_bitcmp1_b32 s100, 24
	s_cbranch_scc0 .Lcv_regular
	s_mov_b32 s11, 1

; __device__ __forceinline__ void wg_conv_item(Frame& F, int l, int it) {
;     if (it < 208) { const int kt = it / 26, nt = it % 26;
;         wg_convert_tile(F, F.in[3] + (size_t)l * D * INW, INW, WSP(bf16_t, WS_WIN + l * SZ_WIN), D, 256 * kt, 256 * nt, -1, nullptr); return; }
;     it -= 208;
;     if (it < 320) { const int which = it / 64, rr = it % 64, kt = rr / 8, nt = rr % 8;
;         const int src = which == 0 ? 10 : 12 + which;
;         const size_t dst = which == 0 ? WS_WOUT : (which == 1 ? WS_WCQ : (which == 2 ? WS_WCK : (which == 3 ? WS_WCV : WS_WCO)));
;         wg_convert_tile(F, F.in[src] + (size_t)l * D * D, D, WSP(bf16_t, dst + l * SZ_SQ), D, 256 * kt, 256 * nt, -1, which == 1 ? F.in[11] + l * D : nullptr); return; }
;     it -= 320;
;     const int e = it / 48, rr = it % 48, kind = rr / 16, item = rr % 16;
;     if (kind < 2) { const int kt = item / 2, nt = item % 2;
.Lcv_item:
	s_bitcmp1_b32 s100, 24
	s_cbranch_scc1 .Lcv_special
	s_cmp_ge_u32 s101, 6
	s_cselect_b32 s57, 1, 0
	s_mul_i32 s14, s57, 6
	s_sub_i32 s14, s101, s14
	s_lshl_b32 s14, s14, 8
	s_add_i32 s14, s14, s9
	s_xor_b32 s56, s57, 1
	s_mul_i32 s56, s56, 0x210
	s_add_i32 s14, s14, s56
	s_branch .Lcv_dec
.Lcv_special:
	s_bitcmp1_b32 s100, 25
	s_cbranch_scc1 .Lcv_sp1
	s_mov_b32 s57, 0
	s_and_b32 s14, s9, 1
	s_lshl_b32 s14, s14, 3
	s_lshr_b32 s56, s9, 5
	s_add_i32 s14, s14, s56
	s_addk_i32 s14, 0x200
	s_branch .Lcv_dec
.Lcv_sp1:
	s_mov_b32 s57, 1
	s_lshr_b32 s14, s9, 5
	s_lshl_b32 s14, s14, 1
	s_and_b32 s56, s9, 1
	s_add_i32 s14, s14, s56
	s_addk_i32 s14, 0x800
.Lcv_dec:
	s_mov_b32 s67, 0
	s_mov_b64 s[70:71], 0
	s_movk_i32 s55, 0x1000
	s_cmpk_lt_u32 s14, 0xd0
	s_cbranch_scc1 .Lcv_A
	s_cmpk_lt_u32 s14, 0x210
	s_cbranch_scc1 .Lcv_B
	s_sub_i32 s76, s14, 0x210
	s_mul_i32 s83, s76, 0xaaab
	s_lshr_b32 s83, s83, 21
	s_mul_i32 s95, s83, 48
	s_sub_i32 s76, s76, s95
	s_lshr_b32 s95, s76, 4
	s_and_b32 s76, s76, 15
	s_lshl_b32 s99, s57, 5
	s_add_i32 s99, s99, s83
	s_lshl_b32 s99, s99, 22
	s_cmp_eq_u32 s95, 2
	s_cbranch_scc1 .Lcv_C2
	s_lshl_b32 s98, s95, 3
	s_addk_i32 s98, 0xc0
	s_load_dwordx2 s[96:97], s[6:7], s98 offset:0x0
	s_load_dwordx2 s[70:71], s[6:7], 0x98
	s_lshr_b32 s98, s76, 1
	s_and_b32 s76, s76, 1
	s_lshl_b32 s14, s98, 19
	s_add_u32 s99, s99, s14
	s_lshl_b32 s14, s76, 10
	s_add_u32 s99, s99, s14
	s_movk_i32 s32, 0x800
	s_lshl_b32 s14, s83, 22
	s_add_u32 s14, s14, 0x8500000
	s_lshl_b32 s56, s57, 27
	s_add_u32 s14, s14, s56
	s_lshl_b32 s76, s76, 21
	s_add_u32 s14, s14, s76
	s_lshl_b32 s95, s95, 19
	s_add_u32 s14, s14, s95
	s_lshl_b32 s76, s98, 9
	s_add_u32 s95, s14, s76
	s_mov_b32 s76, s98
	s_mov_b32 s67, 1
	s_lshl_b32 s56, s57, 13
	s_waitcnt lgkmcnt(0)
	s_add_u32 s70, s70, s56
	s_addc_u32 s71, s71, 0
	s_branch .Lcv_go

; __device__ __forceinline__ void wg_conv_item(Frame& F, int l, int it) {
;     ...
;     if (it < 320) { const int which = it / 64, rr = it % 64, kt = rr / 8, nt = rr % 8;
;         const int src = which == 0 ? 10 : 12 + which;
;         const size_t dst = which == 0 ? WS_WOUT : (which == 1 ? WS_WCQ : (which == 2 ? WS_WCK : (which == 3 ? WS_WCV : WS_WCO)));
;         wg_convert_tile(F, F.in[src] + (size_t)l * D * D, D, WSP(bf16_t, dst + l * SZ_SQ), D, 256 * kt, 256 * nt, -1, which == 1 ? F.in[11] + l * D : nullptr); return; }
.Lcv_B:
	s_sub_i32 s76, s14, 0xd0
	s_lshr_b32 s83, s76, 6
	s_and_b32 s76, s76, 63
	s_lshl_b32 s98, s83, 3
	s_addk_i32 s98, 0x60
	s_cmp_eq_u32 s83, 0
	s_cselect_b32 s98, 0x50, s98
	s_load_dwordx2 s[96:97], s[6:7], s98 offset:0x0
	s_cmp_eq_u32 s83, 1
	s_cbranch_scc0 .Lcv_B_nogain
	s_load_dwordx2 s[70:71], s[6:7], 0x58
	s_lshl_b32 s56, s57, 13
	s_waitcnt lgkmcnt(0)
	s_add_u32 s70, s70, s56
	s_addc_u32 s71, s71, 0
.Lcv_B_nogain:
	s_and_b32 s14, s76, 7
	s_lshr_b32 s76, s76, 3
	s_lshl_b32 s99, s76, 21
	s_lshl_b32 s98, s14, 10
	s_add_u32 s99, s99, s98
	s_lshl_b32 s56, s57, 24
	s_add_u32 s99, s99, s56
	s_movk_i32 s32, 0x2000
	s_lshl_b32 s95, s83, 24
	s_add_u32 s95, s95, 0x3500000
	s_lshl_b32 s56, s57, 23
	s_add_u32 s95, s95, s56
	s_lshl_b32 s14, s14, 20
	s_add_u32 s95, s95, s14
	s_lshl_b32 s14, s76, 9
	s_add_u32 s95, s95, s14
	s_waitcnt lgkmcnt(0)

; #define LAS __attribute__((address_space(3)))
; #define SB() __builtin_amdgcn_sched_barrier(0)
; __device__ __forceinline__ unsigned cvt_pk_bf16(float lo, float hi) { unsigned r; asm volatile("v_cvt_pk_bf16_f32 %0, %1, %2" : "=v"(r) : "v"(lo), "v"(hi)); return r; }
; __device__ __forceinline__ void wg_convert_tile(Frame& F, const float* W, int ldw, bf16_t* WT, int Kd, int k0, int n0, int kind, const float* kgain) {
;     ...
;     f32x4 ld[2][8];
; #pragma unroll
;     for (int j = 0; j < 8; ++j) ld[0][j] = __builtin_nontemporal_load((const f32x4*)(src + (size_t)j * ldw));
; #pragma unroll
;     for (int p = 0; p < 4; ++p) {
;         if (p < 3) {
; #pragma unroll
;             for (int j = 0; j < 8; ++j) ld[(p + 1) & 1][j] = __builtin_nontemporal_load((const f32x4*)(src + (size_t)(64 * (p + 1) + j) * ldw)); }
;         float g[8];
; #pragma unroll
;         for (int j = 0; j < 8; ++j) g[j] = kgain ? kgain[k0 + 64 * p + 8 * w + j] : 1.f;
;         SB();
;         const unsigned kc = (unsigned)(8 * p + w);
; #pragma unroll
;         for (int c = 0; c < 4; ++c) { const int n = 4 * lane + c;
;             u32x4 o; o.x = cvt_pk_bf16(ld[p & 1][0][c] * g[0], ld[p & 1][1][c] * g[1]); o.y = cvt_pk_bf16(ld[p & 1][2][c] * g[2], ld[p & 1][3][c] * g[3]);
;                      o.z = cvt_pk_bf16(ld[p & 1][4][c] * g[4], ld[p & 1][5][c] * g[5]); o.w = cvt_pk_bf16(ld[p & 1][6][c] * g[6], ld[p & 1][7][c] * g[7]);
;             *(LAS u32x4*)(img + n * 512 + ((kc ^ (unsigned)(lane & 31)) << 4)) = o; }
;         SB();
;     }
.Lcv_nogain:
	s_barrier
	s_mov_b64 s[80:81], s[38:39]
	s_mul_i32 s98, s32, 56
	global_load_dwordx4 v[96:99], v3, s[80:81] nt
	s_add_u32 s80, s80, s32
	s_addc_u32 s81, s81, 0
	global_load_dwordx4 v[100:103], v3, s[80:81] nt
	s_add_u32 s80, s80, s32
	s_addc_u32 s81, s81, 0
	global_load_dwordx4 v[104:107], v3, s[80:81] nt
	s_add_u32 s80, s80, s32
	s_addc_u32 s81, s81, 0
	global_load_dwordx4 v[108:111], v3, s[80:81] nt
	s_add_u32 s80, s80, s32
	s_addc_u32 s81, s81, 0
	global_load_dwordx4 v[112:115], v3, s[80:81] nt
	s_add_u32 s80, s80, s32
	s_addc_u32 s81, s81, 0
	global_load_dwordx4 v[116:119], v3, s[80:81] nt
	s_add_u32 s80, s80, s32
	s_addc_u32 s81, s81, 0
	global_load_dwordx4 v[120:123], v3, s[80:81] nt
	s_add_u32 s80, s80, s32
	s_addc_u32 s81, s81, 0
	global_load_dwordx4 v[124:127], v3, s[80:81] nt
	s_add_u32 s80, s80, s32
	s_addc_u32 s81, s81, 0
	s_add_u32 s80, s80, s98
	s_addc_u32 s81, s81, 0
	global_load_dwordx4 v[128:131], v3, s[80:81] nt
	s_add_u32 s80, s80, s32
	s_addc_u32 s81, s81, 0
	global_load_dwordx4 v[132:135], v3, s[80:81] nt
	s_add_u32 s80, s80, s32
	s_addc_u32 s81, s81, 0
	global_load_dwordx4 v[136:139], v3, s[80:81] nt
	s_add_u32 s80, s80, s32
	s_addc_u32 s81, s81, 0
	global_load_dwordx4 v[140:143], v3, s[80:81] nt
	s_add_u32 s80, s80, s32
	s_addc_u32 s81, s81, 0
	global_load_dwordx4 v[144:147], v3, s[80:81] nt
	s_add_u32 s80, s80, s32
	s_addc_u32 s81, s81, 0
	global_load_dwordx4 v[148:151], v3, s[80:81] nt
	s_add_u32 s80, s80, s32
	s_addc_u32 s81, s81, 0
	global_load_dwordx4 v[152:155], v3, s[80:81] nt
	s_add_u32 s80, s80, s32
	s_addc_u32 s81, s81, 0
	global_load_dwordx4 v[156:159], v3, s[80:81] nt
	s_add_u32 s80, s80, s32
	s_addc_u32 s81, s81, 0
	s_add_u32 s80, s80, s98
	s_addc_u32 s81, s81, 0
	global_load_dwordx4 v[160:163], v3, s[80:81] nt
	s_add_u32 s80, s80, s32
	s_addc_u32 s81, s81, 0
	global_load_dwordx4 v[164:167], v3, s[80:81] nt
	s_add_u32 s80, s80, s32
	s_addc_u32 s81, s81, 0
	global_load_dwordx4 v[168:171], v3, s[80:81] nt
	s_add_u32 s80, s80, s32
	s_addc_u32 s81, s81, 0
	global_load_dwordx4 v[172:175], v3, s[80:81] nt
	s_add_u32 s80, s80, s32
	s_addc_u32 s81, s81, 0
	global_load_dwordx4 v[176:179], v3, s[80:81] nt
	s_add_u32 s80, s80, s32
	s_addc_u32 s81, s81, 0
	global_load_dwordx4 v[180:183], v3, s[80:81] nt
	s_add_u32 s80, s80, s32
	s_addc_u32 s81, s81, 0
	global_load_dwordx4 v[184:187], v3, s[80:81] nt
	s_add_u32 s80, s80, s32
	s_addc_u32 s81, s81, 0
	global_load_dwordx4 v[188:191], v3, s[80:81] nt
	s_add_u32 s80, s80, s32
	s_addc_u32 s81, s81, 0
	s_add_u32 s80, s80, s98
	s_addc_u32 s81, s81, 0
	global_load_dwordx4 v[192:195], v3, s[80:81] nt
	s_add_u32 s80, s80, s32
	s_addc_u32 s81, s81, 0
	global_load_dwordx4 v[196:199], v3, s[80:81] nt
	s_add_u32 s80, s80, s32
	s_addc_u32 s81, s81, 0
	global_load_dwordx4 v[200:203], v3, s[80:81] nt
	s_add_u32 s80, s80, s32
	s_addc_u32 s81, s81, 0
	global_load_dwordx4 v[204:207], v3, s[80:81] nt
	s_add_u32 s80, s80, s32
	s_addc_u32 s81, s81, 0
	global_load_dwordx4 v[208:211], v3, s[80:81] nt
	s_add_u32 s80, s80, s32
	s_addc_u32 s81, s81, 0
	global_load_dwordx4 v[212:215], v3, s[80:81] nt
	s_add_u32 s80, s80, s32
	s_addc_u32 s81, s81, 0
	global_load_dwordx4 v[20:23], v3, s[80:81] nt
	s_add_u32 s80, s80, s32
	s_addc_u32 s81, s81, 0
	global_load_dwordx4 v[24:27], v3, s[80:81] nt
	s_waitcnt vmcnt(24)
	s_add_i32 s99, s8, 0
	v_xor_b32_e32 v5, s99, v14
	v_lshlrev_b32_e32 v5, 4, v5
	v_lshl_add_u32 v5, v2, 11, v5
	v_mul_f32_e32 v12, v28, v96
	v_mul_f32_e32 v13, v29, v100
	v_cvt_pk_bf16_f32 v8, v12, v13
	v_mul_f32_e32 v12, v30, v104
	v_mul_f32_e32 v13, v31, v108
	v_cvt_pk_bf16_f32 v9, v12, v13
	v_mul_f32_e32 v12, v32, v112
	v_mul_f32_e32 v13, v33, v116
	v_cvt_pk_bf16_f32 v10, v12, v13
	v_mul_f32_e32 v12, v34, v120
	v_mul_f32_e32 v13, v35, v124
	v_cvt_pk_bf16_f32 v11, v12, v13
	ds_write_b128 v5, v[8:11]
	v_mul_f32_e32 v12, v28, v97
	v_mul_f32_e32 v13, v29, v101
	v_cvt_pk_bf16_f32 v8, v12, v13
	v_mul_f32_e32 v12, v30, v105
	v_mul_f32_e32 v13, v31, v109
	v_cvt_pk_bf16_f32 v9, v12, v13
	v_mul_f32_e32 v12, v32, v113
	v_mul_f32_e32 v13, v33, v117
	v_cvt_pk_bf16_f32 v10, v12, v13
	v_mul_f32_e32 v12, v34, v121
	v_mul_f32_e32 v13, v35, v125
	v_cvt_pk_bf16_f32 v11, v12, v13
	ds_write_b128 v5, v[8:11] offset:512
	v_mul_f32_e32 v12, v28, v98
	v_mul_f32_e32 v13, v29, v102
	v_cvt_pk_bf16_f32 v8, v12, v13
	v_mul_f32_e32 v12, v30, v106
	v_mul_f32_e32 v13, v31, v110
	v_cvt_pk_bf16_f32 v9, v12, v13
	v_mul_f32_e32 v12, v32, v114
	v_mul_f32_e32 v13, v33, v118
	v_cvt_pk_bf16_f32 v10, v12, v13
	v_mul_f32_e32 v12, v34, v122
	v_mul_f32_e32 v13, v35, v126
	v_cvt_pk_bf16_f32 v11, v12, v13
	ds_write_b128 v5, v[8:11] offset:1024
	v_mul_f32_e32 v12, v28, v99
	v_mul_f32_e32 v13, v29, v103
	v_cvt_pk_bf16_f32 v8, v12, v13
	v_mul_f32_e32 v12, v30, v107
	v_mul_f32_e32 v13, v31, v111
	v_cvt_pk_bf16_f32 v9, v12, v13
	v_mul_f32_e32 v12, v32, v115
	v_mul_f32_e32 v13, v33, v119
	v_cvt_pk_bf16_f32 v10, v12, v13
	v_mul_f32_e32 v12, v34, v123
	v_mul_f32_e32 v13, v35, v127
	v_cvt_pk_bf16_f32 v11, v12, v13
	ds_write_b128 v5, v[8:11] offset:1536
	s_waitcnt vmcnt(16)
; #define LAS __attribute__((address_space(3)))
; #define SB() __builtin_amdgcn_sched_barrier(0)
; __device__ __forceinline__ unsigned cvt_pk_bf16(float lo, float hi) { unsigned r; asm volatile("v_cvt_pk_bf16_f32 %0, %1, %2" : "=v"(r) : "v"(lo), "v"(hi)); return r; }
; __device__ __forceinline__ void wg_convert_tile(Frame& F, const float* W, int ldw, bf16_t* WT, int Kd, int k0, int n0, int kind, const float* kgain) {
;     ...
; #pragma unroll
;     for (int p = 0; p < 4; ++p) {
;         if (p < 3) {
; #pragma unroll
;             for (int j = 0; j < 8; ++j) ld[(p + 1) & 1][j] = __builtin_nontemporal_load((const f32x4*)(src + (size_t)(64 * (p + 1) + j) * ldw)); }
;         float g[8];
; #pragma unroll
;         for (int j = 0; j < 8; ++j) g[j] = kgain ? kgain[k0 + 64 * p + 8 * w + j] : 1.f;
;         SB();
;         const unsigned kc = (unsigned)(8 * p + w);
; #pragma unroll
;         for (int c = 0; c < 4; ++c) { const int n = 4 * lane + c;
;             u32x4 o; o.x = cvt_pk_bf16(ld[p & 1][0][c] * g[0], ld[p & 1][1][c] * g[1]); o.y = cvt_pk_bf16(ld[p & 1][2][c] * g[2], ld[p & 1][3][c] * g[3]);
;                      o.z = cvt_pk_bf16(ld[p & 1][4][c] * g[4], ld[p & 1][5][c] * g[5]); o.w = cvt_pk_bf16(ld[p & 1][6][c] * g[6], ld[p & 1][7][c] * g[7]);
;             *(LAS u32x4*)(img + n * 512 + ((kc ^ (unsigned)(lane & 31)) << 4)) = o; }
;         SB();
;     }
	s_add_i32 s99, s8, 8
	v_xor_b32_e32 v5, s99, v14
	v_lshlrev_b32_e32 v5, 4, v5
	v_lshl_add_u32 v5, v2, 11, v5
	v_mul_f32_e32 v12, v36, v128
	v_mul_f32_e32 v13, v37, v132
	v_cvt_pk_bf16_f32 v8, v12, v13
	v_mul_f32_e32 v12, v38, v136
	v_mul_f32_e32 v13, v39, v140
	v_cvt_pk_bf16_f32 v9, v12, v13
	v_mul_f32_e32 v12, v40, v144
	v_mul_f32_e32 v13, v41, v148
	v_cvt_pk_bf16_f32 v10, v12, v13
	v_mul_f32_e32 v12, v42, v152
	v_mul_f32_e32 v13, v43, v156
	v_cvt_pk_bf16_f32 v11, v12, v13
	ds_write_b128 v5, v[8:11]
	v_mul_f32_e32 v12, v36, v129
	v_mul_f32_e32 v13, v37, v133
	v_cvt_pk_bf16_f32 v8, v12, v13
	v_mul_f32_e32 v12, v38, v137
	v_mul_f32_e32 v13, v39, v141
	v_cvt_pk_bf16_f32 v9, v12, v13
	v_mul_f32_e32 v12, v40, v145
	v_mul_f32_e32 v13, v41, v149
	v_cvt_pk_bf16_f32 v10, v12, v13
	v_mul_f32_e32 v12, v42, v153
	v_mul_f32_e32 v13, v43, v157
	v_cvt_pk_bf16_f32 v11, v12, v13
	ds_write_b128 v5, v[8:11] offset:512
	v_mul_f32_e32 v12, v36, v130
	v_mul_f32_e32 v13, v37, v134
	v_cvt_pk_bf16_f32 v8, v12, v13
	v_mul_f32_e32 v12, v38, v138
	v_mul_f32_e32 v13, v39, v142
	v_cvt_pk_bf16_f32 v9, v12, v13
	v_mul_f32_e32 v12, v40, v146
	v_mul_f32_e32 v13, v41, v150
	v_cvt_pk_bf16_f32 v10, v12, v13
	v_mul_f32_e32 v12, v42, v154
	v_mul_f32_e32 v13, v43, v158
	v_cvt_pk_bf16_f32 v11, v12, v13
	ds_write_b128 v5, v[8:11] offset:1024
	v_mul_f32_e32 v12, v36, v131
	v_mul_f32_e32 v13, v37, v135
	v_cvt_pk_bf16_f32 v8, v12, v13
	v_mul_f32_e32 v12, v38, v139
	v_mul_f32_e32 v13, v39, v143
	v_cvt_pk_bf16_f32 v9, v12, v13
	v_mul_f32_e32 v12, v40, v147
	v_mul_f32_e32 v13, v41, v151
	v_cvt_pk_bf16_f32 v10, v12, v13
	v_mul_f32_e32 v12, v42, v155
	v_mul_f32_e32 v13, v43, v159
	v_cvt_pk_bf16_f32 v11, v12, v13
	ds_write_b128 v5, v[8:11] offset:1536
	s_waitcnt vmcnt(8)
	s_add_i32 s99, s8, 16
	v_xor_b32_e32 v5, s99, v14
	v_lshlrev_b32_e32 v5, 4, v5
	v_lshl_add_u32 v5, v2, 11, v5
	v_mul_f32_e32 v12, v44, v160
	v_mul_f32_e32 v13, v45, v164
	v_cvt_pk_bf16_f32 v8, v12, v13
	v_mul_f32_e32 v12, v46, v168
	v_mul_f32_e32 v13, v47, v172
	v_cvt_pk_bf16_f32 v9, v12, v13
	v_mul_f32_e32 v12, v50, v176
	v_mul_f32_e32 v13, v51, v180
	v_cvt_pk_bf16_f32 v10, v12, v13
	v_mul_f32_e32 v12, v52, v184
	v_mul_f32_e32 v13, v53, v188
	v_cvt_pk_bf16_f32 v11, v12, v13
	ds_write_b128 v5, v[8:11]
	v_mul_f32_e32 v12, v44, v161
	v_mul_f32_e32 v13, v45, v165
	v_cvt_pk_bf16_f32 v8, v12, v13
	v_mul_f32_e32 v12, v46, v169
	v_mul_f32_e32 v13, v47, v173
	v_cvt_pk_bf16_f32 v9, v12, v13
	v_mul_f32_e32 v12, v50, v177
	v_mul_f32_e32 v13, v51, v181
	v_cvt_pk_bf16_f32 v10, v12, v13
	v_mul_f32_e32 v12, v52, v185
	v_mul_f32_e32 v13, v53, v189
	v_cvt_pk_bf16_f32 v11, v12, v13
	ds_write_b128 v5, v[8:11] offset:512
	v_mul_f32_e32 v12, v44, v162
	v_mul_f32_e32 v13, v45, v166
	v_cvt_pk_bf16_f32 v8, v12, v13
	v_mul_f32_e32 v12, v46, v170
	v_mul_f32_e32 v13, v47, v174
	v_cvt_pk_bf16_f32 v9, v12, v13
	v_mul_f32_e32 v12, v50, v178
	v_mul_f32_e32 v13, v51, v182
	v_cvt_pk_bf16_f32 v10, v12, v13
	v_mul_f32_e32 v12, v52, v186
	v_mul_f32_e32 v13, v53, v190
	v_cvt_pk_bf16_f32 v11, v12, v13
	ds_write_b128 v5, v[8:11] offset:1024
	v_mul_f32_e32 v12, v44, v163
	v_mul_f32_e32 v13, v45, v167
	v_cvt_pk_bf16_f32 v8, v12, v13
	v_mul_f32_e32 v12, v46, v171
	v_mul_f32_e32 v13, v47, v175
	v_cvt_pk_bf16_f32 v9, v12, v13
	v_mul_f32_e32 v12, v50, v179
	v_mul_f32_e32 v13, v51, v183
	v_cvt_pk_bf16_f32 v10, v12, v13
	v_mul_f32_e32 v12, v52, v187
	v_mul_f32_e32 v13, v53, v191
	v_cvt_pk_bf16_f32 v11, v12, v13
	ds_write_b128 v5, v[8:11] offset:1536
	s_waitcnt vmcnt(0)
	s_add_i32 s99, s8, 24
	v_xor_b32_e32 v5, s99, v14
	v_lshlrev_b32_e32 v5, 4, v5
	v_lshl_add_u32 v5, v2, 11, v5
	v_mul_f32_e32 v12, v54, v192
	v_mul_f32_e32 v13, v55, v196
	v_cvt_pk_bf16_f32 v8, v12, v13
	v_mul_f32_e32 v12, v56, v200
	v_mul_f32_e32 v13, v57, v204
	v_cvt_pk_bf16_f32 v9, v12, v13
	v_mul_f32_e32 v12, v58, v208
	v_mul_f32_e32 v13, v59, v212
	v_cvt_pk_bf16_f32 v10, v12, v13
	v_mul_f32_e32 v12, v60, v20
	v_mul_f32_e32 v13, v61, v24
	v_cvt_pk_bf16_f32 v11, v12, v13
	ds_write_b128 v5, v[8:11]
	v_mul_f32_e32 v12, v54, v193
	v_mul_f32_e32 v13, v55, v197
	v_cvt_pk_bf16_f32 v8, v12, v13
	v_mul_f32_e32 v12, v56, v201
	v_mul_f32_e32 v13, v57, v205
	v_cvt_pk_bf16_f32 v9, v12, v13
	v_mul_f32_e32 v12, v58, v209
	v_mul_f32_e32 v13, v59, v213
	v_cvt_pk_bf16_f32 v10, v12, v13
	v_mul_f32_e32 v12, v60, v21
	v_mul_f32_e32 v13, v61, v25
	v_cvt_pk_bf16_f32 v11, v12, v13
	ds_write_b128 v5, v[8:11] offset:512
	v_mul_f32_e32 v12, v54, v194
	v_mul_f32_e32 v13, v55, v198
	v_cvt_pk_bf16_f32 v8, v12, v13
	v_mul_f32_e32 v12, v56, v202
	v_mul_f32_e32 v13, v57, v206
	v_cvt_pk_bf16_f32 v9, v12, v13
	v_mul_f32_e32 v12, v58, v210
	v_mul_f32_e32 v13, v59, v214
	v_cvt_pk_bf16_f32 v10, v12, v13
	v_mul_f32_e32 v12, v60, v22
	v_mul_f32_e32 v13, v61, v26
	v_cvt_pk_bf16_f32 v11, v12, v13
	ds_write_b128 v5, v[8:11] offset:1024
	v_mul_f32_e32 v12, v54, v195
	v_mul_f32_e32 v13, v55, v199
	v_cvt_pk_bf16_f32 v8, v12, v13
	v_mul_f32_e32 v12, v56, v203
	v_mul_f32_e32 v13, v57, v207
	v_cvt_pk_bf16_f32 v9, v12, v13
	v_mul_f32_e32 v12, v58, v211
	v_mul_f32_e32 v13, v59, v215
	v_cvt_pk_bf16_f32 v10, v12, v13
	v_mul_f32_e32 v12, v60, v23
	v_mul_f32_e32 v13, v61, v27
	v_cvt_pk_bf16_f32 v11, v12, v13
	ds_write_b128 v5, v[8:11] offset:1536
	s_waitcnt lgkmcnt(0)
	s_barrier
; #define LAS __attribute__((address_space(3)))
; #define GAS __attribute__((address_space(1)))
; #define SB() __builtin_amdgcn_sched_barrier(0)
; #define LDS_WAIT() asm volatile("s_waitcnt lgkmcnt(0)" ::: "memory")
; __device__ __forceinline__ void wg_convert_tile(Frame& F, const float* W, int ldw, bf16_t* WT, int Kd, int k0, int n0, int kind, const float* kgain) {
;     ...
;     LDS_WAIT(); __syncthreads();
; #pragma unroll
;     for (int t = 0; t < 16; t += 4) { u32x4 v[4];
; #pragma unroll
;         for (int q = 0; q < 4; ++q) { const int idx = (t + q) * 512 + w * 64 + lane, n = idx >> 5, kc = idx & 31; v[q] = *(const LAS u32x4*)(img + n * 512 + ((kc ^ ((n >> 2) & 31)) << 4)); }
;         SB();
; #pragma unroll
;         for (int q = 0; q < 4; ++q) { const int idx = (t + q) * 512 + w * 64 + lane, n = idx >> 5, kc = idx & 31, nn = n0 + n;
;             const int row = kind < 0 ? nn : ((nn >> 7) * 256 + kind * 128 + (nn & 127));
;             __builtin_nontemporal_store(v[q], (GAS u32x4*)(WT + (size_t)row * Kd + k0 + 8 * kc)); }
;         SB(); }
;     LDS_WAIT(); __syncthreads();
	v_lshlrev_b32_e32 v18, 9, v16
	s_lshr_b32 s83, s8, 1
	s_add_i32 s98, s83, 0
	s_and_b32 s98, s98, 31
	v_xor_b32_e32 v7, s98, v14
	v_lshlrev_b32_e32 v7, 4, v7
	s_mov_b32 s99, 0
	v_add3_u32 v7, v7, v18, s99
	ds_read_b128 v[96:99], v7
	s_add_i32 s98, s83, 4
	s_and_b32 s98, s98, 31
	v_xor_b32_e32 v7, s98, v14
	v_lshlrev_b32_e32 v7, 4, v7
	s_mov_b32 s99, 8192
	v_add3_u32 v7, v7, v18, s99
	ds_read_b128 v[100:103], v7
	s_add_i32 s98, s83, 8
	s_and_b32 s98, s98, 31
	v_xor_b32_e32 v7, s98, v14
	v_lshlrev_b32_e32 v7, 4, v7
	s_mov_b32 s99, 16384
	v_add3_u32 v7, v7, v18, s99
	ds_read_b128 v[104:107], v7
	s_add_i32 s98, s83, 12
	s_and_b32 s98, s98, 31
	v_xor_b32_e32 v7, s98, v14
	v_lshlrev_b32_e32 v7, 4, v7
	s_mov_b32 s99, 24576
	v_add3_u32 v7, v7, v18, s99
	ds_read_b128 v[108:111], v7
	s_waitcnt lgkmcnt(0)
	s_movk_i32 s98, 0
	s_mul_i32 s98, s98, s55
	s_add_u32 s98, s64, s98
	s_addc_u32 s99, s65, 0
	global_store_dwordx4 v6, v[96:99], s[98:99] nt
	s_movk_i32 s98, 16
	s_mul_i32 s98, s98, s55
	s_add_u32 s98, s64, s98
	s_addc_u32 s99, s65, 0
	global_store_dwordx4 v6, v[100:103], s[98:99] nt
	s_movk_i32 s98, 32
	s_mul_i32 s98, s98, s55
	s_add_u32 s98, s64, s98
	s_addc_u32 s99, s65, 0
	global_store_dwordx4 v6, v[104:107], s[98:99] nt
	s_movk_i32 s98, 48
	s_mul_i32 s98, s98, s55
	s_add_u32 s98, s64, s98
	s_addc_u32 s99, s65, 0
	global_store_dwordx4 v6, v[108:111], s[98:99] nt
	s_add_i32 s98, s83, 16
	s_and_b32 s98, s98, 31
	v_xor_b32_e32 v7, s98, v14
	v_lshlrev_b32_e32 v7, 4, v7
	s_mov_b32 s99, 32768
	v_add3_u32 v7, v7, v18, s99
	ds_read_b128 v[96:99], v7
	s_add_i32 s98, s83, 20
	s_and_b32 s98, s98, 31
	v_xor_b32_e32 v7, s98, v14
	v_lshlrev_b32_e32 v7, 4, v7
	s_mov_b32 s99, 40960
	v_add3_u32 v7, v7, v18, s99
	ds_read_b128 v[100:103], v7
	s_add_i32 s98, s83, 24
	s_and_b32 s98, s98, 31
	v_xor_b32_e32 v7, s98, v14
	v_lshlrev_b32_e32 v7, 4, v7
	s_mov_b32 s99, 49152
	v_add3_u32 v7, v7, v18, s99
	ds_read_b128 v[104:107], v7
	s_add_i32 s98, s83, 28
	s_and_b32 s98, s98, 31
	v_xor_b32_e32 v7, s98, v14
	v_lshlrev_b32_e32 v7, 4, v7
	s_mov_b32 s99, 57344
	v_add3_u32 v7, v7, v18, s99
	ds_read_b128 v[108:111], v7
	s_waitcnt lgkmcnt(0)
	s_movk_i32 s98, 64
	s_mul_i32 s98, s98, s55
	s_add_u32 s98, s64, s98
	s_addc_u32 s99, s65, 0
	global_store_dwordx4 v6, v[96:99], s[98:99] nt
	s_movk_i32 s98, 80
	s_mul_i32 s98, s98, s55
	s_add_u32 s98, s64, s98
	s_addc_u32 s99, s65, 0
	global_store_dwordx4 v6, v[100:103], s[98:99] nt
	s_movk_i32 s98, 96
	s_mul_i32 s98, s98, s55
	s_add_u32 s98, s64, s98
	s_addc_u32 s99, s65, 0
	global_store_dwordx4 v6, v[104:107], s[98:99] nt
	s_movk_i32 s98, 112
	s_mul_i32 s98, s98, s55
	s_add_u32 s98, s64, s98
	s_addc_u32 s99, s65, 0
	global_store_dwordx4 v6, v[108:111], s[98:99] nt
	s_add_i32 s98, s83, 32
	s_and_b32 s98, s98, 31
	v_xor_b32_e32 v7, s98, v14
	v_lshlrev_b32_e32 v7, 4, v7
	s_mov_b32 s99, 65536
	v_add3_u32 v7, v7, v18, s99
	ds_read_b128 v[96:99], v7
	s_add_i32 s98, s83, 36
	s_and_b32 s98, s98, 31
	v_xor_b32_e32 v7, s98, v14
	v_lshlrev_b32_e32 v7, 4, v7
	s_mov_b32 s99, 73728
	v_add3_u32 v7, v7, v18, s99
	ds_read_b128 v[100:103], v7
	s_add_i32 s98, s83, 40
	s_and_b32 s98, s98, 31
	v_xor_b32_e32 v7, s98, v14
	v_lshlrev_b32_e32 v7, 4, v7
	s_mov_b32 s99, 81920
	v_add3_u32 v7, v7, v18, s99
	ds_read_b128 v[104:107], v7
	s_add_i32 s98, s83, 44
	s_and_b32 s98, s98, 31
	v_xor_b32_e32 v7, s98, v14
	v_lshlrev_b32_e32 v7, 4, v7
	s_mov_b32 s99, 90112
	v_add3_u32 v7, v7, v18, s99
	ds_read_b128 v[108:111], v7
	s_waitcnt lgkmcnt(0)
	s_movk_i32 s98, 128
	s_cmp_eq_u32 s67, 1
	s_cselect_b32 s98, 256, s98
	s_mul_i32 s98, s98, s55
	s_add_u32 s98, s64, s98
	s_addc_u32 s99, s65, 0
	global_store_dwordx4 v6, v[96:99], s[98:99] nt
	s_movk_i32 s98, 144
	s_cmp_eq_u32 s67, 1
	s_cselect_b32 s98, 272, s98
	s_mul_i32 s98, s98, s55
	s_add_u32 s98, s64, s98
	s_addc_u32 s99, s65, 0
	global_store_dwordx4 v6, v[100:103], s[98:99] nt
	s_movk_i32 s98, 160
	s_cmp_eq_u32 s67, 1
	s_cselect_b32 s98, 288, s98
	s_mul_i32 s98, s98, s55
	s_add_u32 s98, s64, s98
	s_addc_u32 s99, s65, 0
	global_store_dwordx4 v6, v[104:107], s[98:99] nt
	s_movk_i32 s98, 176
	s_cmp_eq_u32 s67, 1
	s_cselect_b32 s98, 304, s98
	s_mul_i32 s98, s98, s55
	s_add_u32 s98, s64, s98
	s_addc_u32 s99, s65, 0
	global_store_dwordx4 v6, v[108:111], s[98:99] nt
	s_add_i32 s98, s83, 48
	s_and_b32 s98, s98, 31
	v_xor_b32_e32 v7, s98, v14
	v_lshlrev_b32_e32 v7, 4, v7
	s_mov_b32 s99, 98304
	v_add3_u32 v7, v7, v18, s99
	ds_read_b128 v[96:99], v7
	s_add_i32 s98, s83, 52
	s_and_b32 s98, s98, 31
	v_xor_b32_e32 v7, s98, v14
	v_lshlrev_b32_e32 v7, 4, v7
	s_mov_b32 s99, 106496
	v_add3_u32 v7, v7, v18, s99
	ds_read_b128 v[100:103], v7
	s_add_i32 s98, s83, 56
	s_and_b32 s98, s98, 31
	v_xor_b32_e32 v7, s98, v14
	v_lshlrev_b32_e32 v7, 4, v7
	s_mov_b32 s99, 114688
	v_add3_u32 v7, v7, v18, s99
	ds_read_b128 v[104:107], v7
	s_add_i32 s98, s83, 60
	s_and_b32 s98, s98, 31
	v_xor_b32_e32 v7, s98, v14
	v_lshlrev_b32_e32 v7, 4, v7
	s_mov_b32 s99, 122880
	v_add3_u32 v7, v7, v18, s99
	ds_read_b128 v[108:111], v7
	s_waitcnt lgkmcnt(0)
	s_movk_i32 s98, 192
	s_cmp_eq_u32 s67, 1
	s_cselect_b32 s98, 320, s98
	s_mul_i32 s98, s98, s55
	s_add_u32 s98, s64, s98
	s_addc_u32 s99, s65, 0
	global_store_dwordx4 v6, v[96:99], s[98:99] nt
	s_movk_i32 s98, 208
	s_cmp_eq_u32 s67, 1
	s_cselect_b32 s98, 336, s98
	s_mul_i32 s98, s98, s55
	s_add_u32 s98, s64, s98
	s_addc_u32 s99, s65, 0
	global_store_dwordx4 v6, v[100:103], s[98:99] nt
	s_movk_i32 s98, 224
	s_cmp_eq_u32 s67, 1
	s_cselect_b32 s98, 352, s98
	s_mul_i32 s98, s98, s55
	s_add_u32 s98, s64, s98
	s_addc_u32 s99, s65, 0
	global_store_dwordx4 v6, v[104:107], s[98:99] nt
	s_movk_i32 s98, 240
	s_cmp_eq_u32 s67, 1
	s_cselect_b32 s98, 368, s98
	s_mul_i32 s98, s98, s55
	s_add_u32 s98, s64, s98
	s_addc_u32 s99, s65, 0
	global_store_dwordx4 v6, v[108:111], s[98:99] nt
	s_bitcmp1_b32 s100, 24
	s_cbranch_scc1 .Lcv_spinc
	s_add_i32 s101, s101, 1
	s_branch .Lcv_cnt
; #define LDS_WAIT() asm volatile("s_waitcnt lgkmcnt(0)" ::: "memory")
; __device__ __forceinline__ void wg_convert_tile(Frame& F, const float* W, int ldw, bf16_t* WT, int Kd, int k0, int n0, int kind, const float* kgain) {
;     ...
;     LDS_WAIT(); __syncthreads();
.Lcv_spinc:
	s_bitcmp1_b32 s100, 25
	s_cbranch_scc0 .Lcv_cnt
	s_or_b32 s101, s101, 0x100
.Lcv_cnt:
	s_add_i32 s11, s11, -1
	s_cmp_lg_u32 s11, 0
	s_cbranch_scc1 .Lcv_item
	s_waitcnt vmcnt(0)
	s_barrier
	v_readlane_b32 s6, v253, 0
	v_readlane_b32 s7, v253, 1
	v_readlane_b32 s8, v253, 2
	v_readlane_b32 s9, v253, 3
	v_readlane_b32 s11, v253, 4
	v_readlane_b32 s12, v253, 5
	v_readlane_b32 s13, v253, 6
	v_readlane_b32 s14, v253, 7
	v_readlane_b32 s32, v253, 8
	v_readlane_b32 s38, v253, 9
	v_readlane_b32 s39, v253, 10
	v_readlane_b32 s55, v253, 11
	v_readlane_b32 s56, v253, 12
	v_readlane_b32 s57, v253, 13
	v_readlane_b32 s58, v253, 14
	v_readlane_b32 s59, v253, 15
	v_readlane_b32 s60, v253, 16
	v_readlane_b32 s61, v253, 17
	v_readlane_b32 s62, v253, 18
	v_readlane_b32 s63, v253, 19
	v_readlane_b32 s64, v253, 20
	v_readlane_b32 s65, v253, 21
	v_readlane_b32 s67, v253, 22
	v_readlane_b32 s70, v253, 23
	v_readlane_b32 s71, v253, 24
	v_readlane_b32 s76, v253, 25
	v_readlane_b32 s80, v253, 26
	v_readlane_b32 s81, v253, 27
	v_readlane_b32 s83, v253, 28
	v_readlane_b32 s95, v253, 29
	v_readlane_b32 s96, v253, 30
	v_readlane_b32 s97, v253, 31
	v_readlane_b32 s98, v253, 32
	v_readlane_b32 s99, v253, 33
	s_nop 7
	s_and_b32 s100, s100, 0xff
	s_cmp_eq_u32 s100, 0
	s_cbranch_scc1 .Lcv_ret_0
	s_cmp_eq_u32 s100, 1
	s_cbranch_scc1 .Lcv_ret_1
	s_cmp_eq_u32 s100, 2
	s_cbranch_scc1 .Lcv_ret_2
	s_cmp_eq_u32 s100, 3
	s_cbranch_scc1 .Lcv_ret_3
	s_cmp_eq_u32 s100, 4
	s_cbranch_scc1 .Lcv_ret_4
	s_cmp_eq_u32 s100, 5
	s_cbranch_scc1 .Lcv_ret_5
	s_cmp_eq_u32 s100, 6
	s_cbranch_scc1 .Lcv_ret_6
	s_cmp_eq_u32 s100, 7
	s_cbranch_scc1 .Lcv_ret_7
	s_cmp_eq_u32 s100, 8
	s_cbranch_scc1 .Lcv_ret_8
	s_cmp_eq_u32 s100, 9
	s_cbranch_scc1 .Lcv_ret_9
	s_cmp_eq_u32 s100, 10
	s_cbranch_scc1 .Lcv_ret_10
	s_cmp_eq_u32 s100, 11
	s_cbranch_scc1 .Lcv_ret_11
	s_branch .Lcv_ret_12

; __device__ __forceinline__ int moe_t1(int NT, int G) { const int t1 = NT < G / 4 ? NT : G / 4; return (4 * (NT - t1) < G / 2) ? t1 : NT; }
; #define INL(j) (((MK_PHMASK >> (j)) & 1) && INR(pb + (j)))
; __global__ void __launch_bounds__(NTHR, 2) mega_fwd(Args args) {
;     ...
;         for (int sp = 0; sp < 3; ++sp) {
;             if (INL(10 + sp)) {
;                 if (sp == 0) moe_tables(F, l);
;                 const int NT = (int)F.MISC[MT_NT], T1 = moe_t1(NT, F.G), nUW = 4 * (NT - T1), nUR = (nUW + 7) & ~7;
;                 const bool doUp = sp == 0 || (sp == 1 && bx < nUW), doDown = (sp == 1 && bx >= nUR) || sp == 2;
;                 if (doUp) {
.LBB0_1552:
	v_readlane_b32 s100, v251, 3
	s_nop 3
	s_bitcmp1_b32 s100, 3
	s_cbranch_scc1 .Lcv_ret_9
	s_mul_i32 s100, s87, 3
	s_add_i32 s100, s100, 9
	s_min_u32 s100, s100, 14
	s_cmp_ge_u32 s101, s100
	s_cbranch_scc1 .Lcv_ret_9
	s_lshl_b32 s100, s100, 8
	s_or_b32 s100, s100, 9
	s_branch .Lcv_run
.Lcv_ret_9:
	s_cmp_lg_u32 s101, 14
	s_cbranch_scc1 .Lcv_ret_10
	s_cmp_lg_u32 s87, 2
	s_cbranch_scc1 .Lcv_ret_10
	v_readlane_b32 s100, v251, 3
	s_nop 3
	s_bitcmp1_b32 s100, 3
	s_cbranch_scc1 .Lcv_ret_10
	s_bfe_u32 s100, s100, 0x50003
	s_cmp_lt_u32 s100, 30
	s_cbranch_scc1 .Lcv_ret_10
	s_mov_b32 s100, 50331658
	s_branch .Lcv_run

; #define SEAM(k) do { if (INR(k) && INR((k) + 1)) xcd_barrier(bar); F.lane = lane_id_v(); F.tid = F.wave * 64 + F.lane; { int z_; asm volatile("s_mov_b32 %0, 0" : "=s"(z_)); F.ws = args.ws + z_; F.out = args.out + z_; F.ctl = (gu32*)(args.ws + WS_CTL) + z_; F.in = args.in + z_; F.gw = gw0 + z_; } } while (0)
; __global__ void __launch_bounds__(NTHR, 2) mega_fwd(Args args) {
;     ...
;             SEAM(pb + 10 + sp);
.LBB0_1642:
	s_add_i32 s94, s94, 1
	s_cmp_lt_i32 s94, s75
	s_cselect_b64 s[4:5], -1, 0
	s_and_b64 s[4:5], s[70:71], s[4:5]
	s_andn2_b64 vcc, exec, s[4:5]
	s_cbranch_vccnz .LBB0_1551
	v_readlane_b32 s100, v251, 3
	s_nop 3
	s_bitcmp1_b32 s100, 3
	s_cbranch_scc0 .Lcv_ret_11
	s_mul_i32 s100, s87, 3
	s_add_i32 s100, s100, 9
	s_min_u32 s100, s100, 14
	s_cmp_ge_u32 s101, s100
	s_cbranch_scc1 .Lcv_ret_11
	s_lshl_b32 s100, s100, 8
	s_or_b32 s100, s100, 11
	s_branch .Lcv_run
.Lcv_ret_11:
	s_cmp_lg_u32 s101, 14
	s_cbranch_scc1 .Lcv_ret_12
	s_cmp_lg_u32 s87, 2
	s_cbranch_scc1 .Lcv_ret_12
	v_readlane_b32 s100, v251, 3
	s_nop 3
	s_bitcmp1_b32 s100, 3
	s_cbranch_scc0 .Lcv_ret_12
	s_bfe_u32 s100, s100, 0x50003
	s_cmp_lt_u32 s100, 30
	s_cbranch_scc1 .Lcv_ret_12
	s_mov_b32 s100, 50331660
	s_branch .Lcv_run
